# static prio for waves 4-7 in P5/P7, attention ds_write ladders counted for in-order queue, mLSTM barrier before prefetch loads
# speedup vs baseline: 1.0000x; 1.0000x over previous
.LBB0_1095:
	s_cmp_lt_i32 s92, 6
	s_cselect_b64 s[0:1], -1, 0
	s_cmp_gt_i32 s93, 5
	s_cselect_b64 s[2:3], -1, 0
	s_and_b64 s[0:1], s[0:1], s[2:3]
	s_andn2_b64 vcc, exec, s[0:1]
	s_cbranch_vccnz .LBB0_1198
	v_readfirstlane_b32 s98, v0
	s_nop 3
	s_lshr_b32 s98, s98, 8
	s_cmp_eq_u32 s98, 0
	s_cbranch_scc1 .Lprio5_skip
	s_setprio 1
.Lprio5_skip:
	v_mov_b32_e32 v1, v0
	s_cmpk_gt_i32 s90, 0xff
	v_readfirstlane_b32 s0, v1
	s_cbranch_scc1 .LBB0_1148
	s_waitcnt vmcnt(0)
	v_ashrrev_i32_e32 v110, 3, v1
	s_add_u32 s4, s30, 0xa600000
	v_ashrrev_i32_e32 v111, 31, v110
	v_and_b32_e32 v3, 63, v1
	v_bfe_u32 v5, v1, 5, 1
	v_and_b32_e32 v8, 31, v1
	s_addc_u32 s5, s31, 0
	v_mov_b32_e32 v34, 0
	v_lshlrev_b64 v[6:7], 7, v[110:111]
	v_lshlrev_b32_e32 v1, 4, v1
	s_ashr_i32 s0, s0, 5
	v_lshl_add_u64 v[6:7], s[4:5], 0, v[6:7]
	v_and_b32_e32 v112, 0x70, v1
	v_mov_b32_e32 v113, v34
	s_and_b32 s2, s0, -2
	v_lshl_add_u64 v[114:115], v[6:7], 0, v[112:113]
	s_mov_b64 s[0:1], 0x2000
	v_lshl_add_u64 v[116:117], v[114:115], 0, s[0:1]
	s_movk_i32 s0, 0x90
	v_mul_lo_u32 v1, v110, s0
	s_mov_b64 s[0:1], 0x4000
	v_lshlrev_b32_e32 v6, 4, v5
	v_mov_b32_e32 v7, v34
	v_lshlrev_b32_e32 v2, 6, v8
	v_lshlrev_b32_e32 v4, 3, v5
	v_add_u32_e32 v9, 0, v1
	v_lshl_add_u64 v[118:119], v[114:115], 0, s[0:1]
	s_mov_b64 s[0:1], 0x6000
	v_lshl_add_u64 v[122:123], s[4:5], 0, v[112:113]
	v_add_u32_e32 v127, 0, v6
	v_lshl_add_u64 v[6:7], s[30:31], 0, v[6:7]
	s_mov_b64 s[4:5], 0xa700000
	v_add_u32_e32 v111, 0x2400, v1
	v_lshl_add_u64 v[120:121], v[114:115], 0, s[0:1]
	v_cmp_gt_u32_e64 s[0:1], 32, v3
	v_mul_u32_u24_e32 v113, 0x90, v8
	v_lshl_add_u64 v[124:125], v[6:7], 0, s[4:5]
	v_lshlrev_b32_e32 v126, 2, v3
	v_lshlrev_b32_e32 v128, 2, v8
	v_or_b32_e32 v129, s2, v5
	v_lshlrev_b32_e32 v130, 1, v2
	v_mov_b32_e32 v131, v34
	s_waitcnt lgkmcnt(0)
	v_lshlrev_b32_e32 v132, 1, v4
	v_mov_b32_e32 v133, v34
	s_mov_b64 s[4:5], 0x47b08000
	s_mov_b32 s3, 0x47b08000
	v_add_u32_e32 v138, v9, v112
	s_mov_b32 s20, s90
	s_branch .LBB0_1099

.LBB0_1148:
	s_setprio 0
	s_cmp_lt_i32 s93, 7
	s_cbranch_scc1 .LBB0_1198
	s_waitcnt vmcnt(0)
	v_cmp_eq_u32_e32 vcc, 0, v0
	s_waitcnt vmcnt(0) lgkmcnt(0)
	s_barrier
	s_and_saveexec_b64 s[0:1], vcc
	s_cbranch_execz .LBB0_1197
	v_mov_b32_e32 v1, s70
	s_waitcnt vmcnt(0) expcnt(0) lgkmcnt(0)
	ds_read_b32 v3, v1
	ds_read_b32 v1, v1 offset:4
	s_waitcnt lgkmcnt(1)
	v_cmp_ne_u32_e32 vcc, 0, v3
	s_cbranch_vccnz .LBB0_1165
	v_readlane_b32 s4, v254, 0
	v_readlane_b32 s5, v254, 1
	s_load_dwordx2 s[2:3], s[4:5], 0x4
	s_add_u32 s4, s86, 0x1000
	s_addc_u32 s5, s87, 0
	s_add_u32 s6, s86, 0x1100
	s_addc_u32 s7, s87, 0
	s_add_u32 s8, s86, 0x1200
	s_addc_u32 s9, s87, 0
	s_waitcnt lgkmcnt(0)
	s_mul_i32 s2, s2, s84
	s_add_u32 s10, s86, 0x1300
	s_mul_i32 s2, s2, s3
	s_addc_u32 s11, s87, 0
	s_mov_b32 s3, 1
	v_mov_b32_e32 v17, 0
	s_branch .LBB0_1153

.LBB0_1918:
	s_cmp_lt_i32 s92, 8
	s_cselect_b64 s[0:1], -1, 0
	s_cmp_gt_i32 s93, 7
	s_cselect_b64 s[2:3], -1, 0
	s_and_b64 s[0:1], s[0:1], s[2:3]
	s_andn2_b64 vcc, exec, s[0:1]
	s_cbranch_vccnz .LBB0_2249
	v_readfirstlane_b32 s98, v0
	s_nop 3
	s_lshr_b32 s98, s98, 8
	s_cmp_eq_u32 s98, 0
	s_cbranch_scc1 .Lprio7_skip
	s_setprio 1
.Lprio7_skip:
	v_mov_b32_e32 v152, v0
	s_mov_b64 s[4:5], -1
	v_readfirstlane_b32 s0, v152
	s_ashr_i32 s68, s0, 6
	s_cmp_lt_i32 s90, 64
	v_writelane_b32 v254, s0, 51
	s_cselect_b64 s[0:1], -1, 0
	s_cmp_gt_i32 s90, 63
	s_cselect_b64 s[2:3], -1, 0
	v_writelane_b32 v254, s2, 55
	v_and_b32_e32 v1, 63, v152
	s_cmpk_eq_i32 s84, 0x100
	v_writelane_b32 v254, s3, 56
	s_cbranch_scc1 .LBB0_2038
	s_andn2_b64 vcc, exec, s[0:1]
	s_cbranch_vccnz .LBB0_1997
	s_add_u32 s16, s30, 0xb100000
	s_addc_u32 s17, s31, 0
	s_add_u32 s24, s30, 0xd100000
	s_addc_u32 s69, s31, 0
	s_add_u32 s25, s30, 0x6a400000
	s_addc_u32 s72, s31, 0
	v_writelane_b32 v254, s86, 36
	s_add_u32 s73, s30, 0x6ac00000
	s_mov_b32 s2, s90
	v_writelane_b32 v254, s87, 37
	s_addc_u32 s86, s31, 0
	s_add_u32 s87, s30, 0x6ac40000
	s_addc_u32 s88, s31, 0
	v_writelane_b32 v254, s92, 38
	s_add_u32 s89, s30, 0x6ac80000
	s_addc_u32 s90, s31, 0
	v_writelane_b32 v254, s93, 39
	v_writelane_b32 v254, s94, 40
	s_add_u32 s91, s30, 0x6ad00000
	v_writelane_b32 v254, s95, 41
	s_addc_u32 s92, s31, 0
	s_add_u32 s93, s30, 0xa880000
	s_addc_u32 s94, s31, 0
	s_add_u32 s95, s30, 0x29f04e00
	s_addc_u32 s96, s31, 0
	s_mov_b32 s0, s2
	s_add_u32 s97, s30, 0x6ac801fc
	v_writelane_b32 v254, s0, 47
	s_mov_b32 s36, s68
	s_addc_u32 s18, s31, 0
	s_add_i32 s26, 0, 0x10000
	s_mov_b32 s23, 0x20000
	v_writelane_b32 v254, s1, 48
	s_mov_b32 s68, s84
	s_waitcnt vmcnt(0)
	v_mov_b32_e32 v3, 0
	v_mov_b32_e32 v153, 0x3f80
	s_brev_b32 s42, 64
	s_mov_b32 s43, s23
	s_brev_b32 s46, 16
	s_mov_b32 s47, s23
	s_mov_b32 s50, 0x100000
	s_mov_b32 s51, s23
	s_mov_b32 s54, 0x40000
	s_mov_b32 s55, s23
	s_movk_i32 s3, 0x210
	s_add_i32 s35, 0, 0x1a500
	v_mov_b32_e32 v160, s26
	s_mov_b32 s19, s2
	v_writelane_b32 v254, s36, 52
	v_mov_b32_e32 v4, v1
	v_mov_b32_e32 v116, v152
	s_mov_b32 s39, 0
	s_brev_b32 s58, 64
	s_mov_b32 s62, 0x100000
	s_branch .LBB0_1924

.LBB0_2042:
	s_or_b64 exec, exec, s[4:5]
	s_add_u32 s22, s30, 0x47b00000
	s_addc_u32 s23, s31, 0
	s_add_u32 s20, s30, 0x59b00000
	v_readlane_b32 s9, v254, 51
	s_addc_u32 s21, s31, 0
	s_waitcnt vmcnt(0)
	v_and_b32_e32 v15, 15, v152
	s_bfe_u32 s3, s9, 0x10006
	v_lshl_or_b32 v18, s3, 4, v15
	v_add_u32_e32 v2, 1, v18
	v_cvt_f32_ubyte0_e32 v2, v2
	v_mul_f32_e32 v3, 0xbe800000, v2
	s_mov_b32 s4, 0xc2fc0000
	v_mov_b32_e32 v4, 0x42800000
	v_cmp_gt_f32_e32 vcc, s4, v3
	s_ashr_i32 s6, s9, 7
	s_add_u32 s12, s30, 0x9e00000
	v_cndmask_b32_e32 v3, 0, v4, vcc
	v_fmac_f32_e32 v3, 0xbe800000, v2
	v_exp_f32_e32 v2, v3
	s_addc_u32 s4, s31, 0
	s_and_b32 s13, s4, 0xffff
	s_mul_i32 s4, s38, 0x9000
	v_not_b32_e32 v3, 63
	s_mul_hi_i32 s5, s38, 0x9000
	s_add_u32 s4, s22, s4
	v_cndmask_b32_e32 v3, 0, v3, vcc
	s_addc_u32 s5, s23, s5
	v_lshlrev_b32_e32 v10, 10, v18
	v_mov_b32_e32 v11, 0
	v_ldexp_f32 v131, v2, v3
	v_lshl_add_u64 v[2:3], s[4:5], 0, v[10:11]
	s_and_b32 s4, s9, 0xffffff80
	s_ashr_i32 s5, s4, 31
	s_lshl_b64 s[4:5], s[4:5], 1
	s_lshl_b32 s53, s68, 5
	v_lshl_add_u64 v[2:3], v[2:3], 0, s[4:5]
	v_and_b32_e32 v12, 48, v1
	v_mov_b32_e32 v13, v11
	s_add_i32 s54, s53, 0
	v_lshl_add_u64 v[2:3], v[2:3], 0, v[12:13]
	s_add_i32 s54, s54, 0x10400
	global_load_dwordx4 v[34:37], v[2:3], off
	global_load_dwordx4 v[38:41], v[2:3], off offset:64
	global_load_dwordx4 v[42:45], v[2:3], off offset:128
	global_load_dwordx4 v[46:49], v[2:3], off offset:192
	s_waitcnt lgkmcnt(0)
	s_barrier
	v_mov_b32_e32 v19, s54
	ds_read_b128 v[2:5], v19
	ds_read_b128 v[6:9], v19 offset:16
	s_mov_b32 s15, 0x20000
	s_mov_b32 s14, 0x800000
	s_waitcnt lgkmcnt(2)
	v_lshlrev_b32_e32 v132, 4, v1
	s_waitcnt lgkmcnt(1)
	v_readfirstlane_b32 s7, v2
	s_lshl_b32 s7, s7, 10
	v_readfirstlane_b32 s8, v3
	s_lshl_b32 s8, s8, 10
	s_nop 1
	buffer_load_dwordx4 v[50:53], v132, s[12:15], s7 offen
	s_nop 0
	buffer_load_dwordx4 v[54:57], v132, s[12:15], s8 offen
	v_readfirstlane_b32 s7, v4
	s_lshl_b32 s7, s7, 10
	v_readfirstlane_b32 s8, v5
	s_lshl_b32 s8, s8, 10
	s_nop 1
	buffer_load_dwordx4 v[58:61], v132, s[12:15], s7 offen
	s_nop 0
	buffer_load_dwordx4 v[62:65], v132, s[12:15], s8 offen
	s_waitcnt lgkmcnt(0)
	v_readfirstlane_b32 s7, v6
	s_lshl_b32 s7, s7, 10
	v_readfirstlane_b32 s8, v7
	s_lshl_b32 s8, s8, 10
	s_nop 1
	buffer_load_dwordx4 v[66:69], v132, s[12:15], s7 offen
	s_nop 0
	buffer_load_dwordx4 v[70:73], v132, s[12:15], s8 offen
	ds_read_b128 v[2:5], v19 offset:256
	v_readfirstlane_b32 s7, v8
	s_lshl_b32 s7, s7, 10
	v_readfirstlane_b32 s8, v9
	s_lshl_b32 s8, s8, 10
	s_nop 1
	buffer_load_dwordx4 v[82:85], v132, s[12:15], s7 offen
	s_nop 0
	buffer_load_dwordx4 v[86:89], v132, s[12:15], s8 offen
	ds_read_b128 v[6:9], v19 offset:272
	s_waitcnt lgkmcnt(1)
	v_readfirstlane_b32 s7, v2
	s_lshl_b32 s7, s7, 10
	v_readfirstlane_b32 s8, v3
	s_lshl_b32 s8, s8, 10
	s_nop 1
	buffer_load_dwordx4 v[74:77], v132, s[12:15], s7 offen
	s_nop 0
	buffer_load_dwordx4 v[78:81], v132, s[12:15], s8 offen
	v_readfirstlane_b32 s7, v4
	s_lshl_b32 s7, s7, 10
	v_readfirstlane_b32 s8, v5
	s_lshl_b32 s8, s8, 10
	s_nop 1
	buffer_load_dwordx4 v[90:93], v132, s[12:15], s7 offen
	s_nop 0
	buffer_load_dwordx4 v[94:97], v132, s[12:15], s8 offen
	s_waitcnt lgkmcnt(0)
	v_readfirstlane_b32 s7, v6
	s_lshl_b32 s7, s7, 10
	v_readfirstlane_b32 s8, v7
	s_lshl_b32 s8, s8, 10
	s_nop 1
	buffer_load_dwordx4 v[98:101], v132, s[12:15], s7 offen
	s_nop 0
	buffer_load_dwordx4 v[102:105], v132, s[12:15], s8 offen
	v_readfirstlane_b32 s7, v8
	s_lshl_b32 s7, s7, 10
	v_readfirstlane_b32 s8, v9
	s_lshl_b32 s8, s8, 10
	s_nop 1
	buffer_load_dwordx4 v[106:109], v132, s[12:15], s7 offen
	s_nop 0
	buffer_load_dwordx4 v[110:113], v132, s[12:15], s8 offen
	s_lshl_b32 s7, s6, 8
	s_add_i32 s34, 0, 0x10c00
	s_add_i32 s7, s7, 0
	s_cmp_gt_i32 s6, 0
	s_cselect_b64 s[40:41], -1, 0
	s_lshl_b32 s6, s68, 8
	s_add_i32 s6, s6, 0xffffe00
	v_lshl_add_u64 v[2:3], s[22:23], 0, v[10:11]
	s_cmp_lt_i32 s68, 2
	v_and_b32_e32 v5, 48, v152
	v_or_b32_e32 v7, s6, v1
	v_lshl_add_u64 v[2:3], v[2:3], 0, s[4:5]
	s_cselect_b64 s[42:43], -1, 0
	s_lshl_b32 s6, s3, 12
	s_add_i32 s3, 0, 0x11500
	v_and_b32_e32 v16, 31, v152
	v_add_u32_e32 v6, s7, v5
	v_lshl_add_u64 v[134:135], v[2:3], 0, v[12:13]
	s_movk_i32 s7, 0x90
	v_mov_b32_e32 v3, s3
	v_lshlrev_b32_e32 v10, 2, v1
	v_add_u32_e32 v148, s34, v5
	v_mad_u32_u24 v5, v18, s7, v3
	v_mad_u32_u24 v155, v16, s7, v3
	s_and_b32 s7, s9, 0x7fffffc0
	v_and_b32_e32 v9, 16, v152
	v_and_b32_e32 v10, 12, v10
	v_or3_b32 v9, s7, v9, v10
	v_mov_b32_e32 v133, v11
	v_ashrrev_i32_e32 v11, 6, v152
	s_movk_i32 s7, 0x410
	v_mul_lo_u32 v12, v11, s7
	v_lshlrev_b32_e32 v140, 9, v11
	v_add_u32_e32 v11, 0x200, v152
	v_ashrrev_i32_e32 v11, 6, v11
	v_lshrrev_b32_e32 v17, 5, v1
	s_add_i32 s50, 0, 0x11400
	v_lshlrev_b32_e32 v8, 2, v18
	s_add_i32 s51, 0, 0x11480
	v_mul_lo_u32 v23, v11, s7
	v_lshlrev_b32_e32 v142, 9, v11
	v_add_u32_e32 v11, 0x400, v152
	v_lshrrev_b32_e32 v14, 4, v1
	v_add_u32_e32 v150, s50, v8
	v_add_u32_e32 v151, s51, v8
	v_lshlrev_b32_e32 v3, 3, v17
	v_bfe_u32 v8, v152, 2, 2
	s_lshl_b32 s9, s68, 7
	v_ashrrev_i32_e32 v11, 6, v11
	v_lshlrev_b32_e32 v20, 3, v14
	v_lshlrev_b32_e32 v149, 2, v14
	v_mul_u32_u24_e32 v13, 0x410, v15
	v_or_b32_e32 v14, v3, v8
	v_or_b32_e32 v15, 16, v3
	v_or_b32_e32 v19, 32, v3
	v_or_b32_e32 v3, 48, v3
	s_add_i32 s10, s3, s9
	s_add_i32 s9, s9, 0
	v_mul_lo_u32 v24, v11, s7
	v_lshlrev_b32_e32 v144, 9, v11
	v_add_u32_e32 v11, 0x600, v152
	s_add_i32 s35, 0, 0x12700
	v_lshlrev_b32_e32 v18, 1, v15
	v_or_b32_e32 v15, v15, v8
	v_lshlrev_b32_e32 v21, 1, v19
	v_or_b32_e32 v19, v19, v8
	v_lshlrev_b32_e32 v22, 1, v3
	v_or_b32_e32 v3, v3, v8
	v_lshlrev_b32_e32 v8, 1, v16
	s_add_i32 s9, s9, 0x11540
	v_ashrrev_i32_e32 v11, 6, v11
	v_add_u32_e32 v4, 0, v132
	v_add_u32_e32 v2, s35, v132
	v_lshlrev_b32_e32 v154, 4, v17
	v_add_u32_e32 v10, s3, v132
	s_mul_i32 s8, s68, 0x2080
	v_lshlrev_b32_e32 v7, 4, v7
	v_lshlrev_b32_e32 v9, 1, v9
	v_mad_u32_u24 v14, v14, s7, 0
	v_mad_u32_u24 v15, v15, s7, 0
	v_mad_u32_u24 v19, v19, s7, 0
	v_mad_u32_u24 v3, v3, s7, 0
	v_add_u32_e32 v16, s10, v8
	v_mul_u32_u24_e32 v17, 0x1040, v17
	v_add_u32_e32 v8, s9, v8
	v_mul_lo_u32 v25, v11, s7
	v_lshlrev_b32_e32 v146, 9, v11
	s_mov_b32 s52, 0
	v_cmp_gt_u32_e64 s[4:5], 16, v1
	v_lshl_add_u64 v[136:137], v[152:153], 2, s[18:19]
	v_lshl_add_u64 v[138:139], s[20:21], 0, v[132:133]
	v_or_b32_e32 v133, 0x73, v149
	v_or_b32_e32 v153, 0x80, v149
	v_or_b32_e32 v156, 0x81, v149
	v_or_b32_e32 v157, 0x82, v149
	v_or_b32_e32 v158, 0x83, v149
	v_or_b32_e32 v159, 0x90, v149
	v_or_b32_e32 v160, 0x91, v149
	v_or_b32_e32 v161, 0x92, v149
	v_or_b32_e32 v162, 0x93, v149
	v_or_b32_e32 v163, 0xa0, v149
	v_or_b32_e32 v164, 0xa1, v149
	v_or_b32_e32 v165, 0xa2, v149
	v_or_b32_e32 v166, 0xa3, v149
	v_or_b32_e32 v167, 0xb0, v149
	v_or_b32_e32 v168, 0xb1, v149
	v_or_b32_e32 v169, 0xb2, v149
	v_or_b32_e32 v170, 0xb3, v149
	v_or_b32_e32 v171, 0xc0, v149
	v_or_b32_e32 v172, 0xc1, v149
	v_or_b32_e32 v173, 0xc2, v149
	v_or_b32_e32 v174, 0xc3, v149
	v_or_b32_e32 v175, 0xd0, v149
	v_or_b32_e32 v176, 0xd1, v149
	v_or_b32_e32 v177, 0xd2, v149
	v_or_b32_e32 v178, 0xd3, v149
	v_or_b32_e32 v179, 0xe0, v149
	v_or_b32_e32 v180, 0xe1, v149
	v_or_b32_e32 v181, 0xe2, v149
	v_or_b32_e32 v182, 0xe3, v149
	v_or_b32_e32 v183, 0xf0, v149
	v_or_b32_e32 v184, 0xf1, v149
	v_or_b32_e32 v185, 0xf2, v149
	v_or_b32_e32 v186, 0xf3, v149
	v_ashrrev_i32_e32 v141, 31, v140
	v_ashrrev_i32_e32 v143, 31, v142
	v_ashrrev_i32_e32 v145, 31, v144
	v_ashrrev_i32_e32 v147, 31, v146
	v_mov_b32_e32 v130, 0x3db504f3
	s_sub_i32 s55, 0, s90
	s_movk_i32 s56, 0x1f7f
	s_mov_b32 s57, 0xff800000
	v_add_u32_e32 v187, v16, v17
	v_add_u32_e32 v188, v8, v17
	v_add_u32_e32 v189, v10, v12
	v_add_u32_e32 v190, v10, v23
	v_add_u32_e32 v191, v10, v24
	v_add_u32_e32 v192, v10, v25
	v_add_u32_e32 v193, s8, v4
	v_add_u32_e32 v194, v6, v13
	v_add_u32_e32 v195, 0, v7
	v_add_u32_e32 v196, s6, v2
	v_add_u32_e32 v197, v5, v20
	v_mov_b32_e32 v198, 0xff800000
	v_add_u32_e32 v199, v14, v9
	v_add_u32_e32 v200, v155, v18
	v_add_u32_e32 v201, v15, v9
	v_add_u32_e32 v202, v155, v21
	v_add_u32_e32 v203, v19, v9
	v_add_u32_e32 v204, v155, v22
	v_add_u32_e32 v205, v3, v9
	v_mov_b32_e32 v206, 0x9000
	s_mov_b32 s98, 0
	s_branch .LBB0_2045

.LBB0_2044:
	s_waitcnt lgkmcnt(0)
	s_barrier
	ds_read_b128 v[114:117], v216 offset:96
	ds_read_b128 v[118:121], v216 offset:64
	ds_read_b128 v[122:125], v216 offset:32
	ds_read_b128 v[126:129], v216
	s_waitcnt lgkmcnt(3)
	v_pk_mul_f32 v[30:31], v[30:31], v[114:115]
	v_pk_mul_f32 v[32:33], v[32:33], v[116:117]
	v_pk_mul_f32 v[14:15], v[14:15], v[114:115]
	v_pk_mul_f32 v[16:17], v[16:17], v[116:117]
	ds_read_b128 v[114:117], v211
	ds_read_b64_tr_b16 v[210:211], v199
	ds_read_b64_tr_b16 v[212:213], v199 offset:4160
	ds_read_b64_tr_b16 v[216:217], v199 offset:4224
	ds_read_b64_tr_b16 v[214:215], v199 offset:64
	ds_read_b128 v[218:221], v200
	ds_read_b64_tr_b16 v[222:223], v201
	ds_read_b64_tr_b16 v[224:225], v201 offset:4160
	ds_read_b64_tr_b16 v[228:229], v201 offset:4224
	ds_read_b64_tr_b16 v[226:227], v201 offset:64
	s_waitcnt lgkmcnt(12)
	v_pk_mul_f32 v[26:27], v[26:27], v[118:119]
	s_waitcnt lgkmcnt(11)
	v_pk_mul_f32 v[22:23], v[22:23], v[122:123]
	v_pk_mul_f32 v[28:29], v[28:29], v[120:121]
	v_pk_mul_f32 v[24:25], v[24:25], v[124:125]
	s_waitcnt lgkmcnt(10)
	v_pk_mul_f32 v[20:21], v[20:21], v[128:129]
	v_pk_mul_f32 v[18:19], v[18:19], v[126:127]
	v_pk_mul_f32 v[10:11], v[10:11], v[118:119]
	v_pk_mul_f32 v[6:7], v[6:7], v[122:123]
	v_pk_mul_f32 v[12:13], v[12:13], v[120:121]
	v_pk_mul_f32 v[8:9], v[8:9], v[124:125]
	v_pk_mul_f32 v[4:5], v[4:5], v[128:129]
	v_pk_mul_f32 v[2:3], v[2:3], v[126:127]
	s_waitcnt lgkmcnt(7)
	v_mfma_f32_32x32x16_bf16 v[18:33], v[114:117], v[210:213], v[18:33]
	s_waitcnt lgkmcnt(5)
	v_mfma_f32_32x32x16_bf16 v[2:17], v[114:117], v[214:217], v[2:17]
	s_waitcnt lgkmcnt(2)
	v_mfma_f32_32x32x16_bf16 v[18:33], v[218:221], v[222:225], v[18:33]
	s_waitcnt lgkmcnt(0)
	v_mfma_f32_32x32x16_bf16 v[2:17], v[218:221], v[226:229], v[2:17]
	ds_read_b128 v[114:117], v202
	ds_read_b64_tr_b16 v[118:119], v203
	ds_read_b64_tr_b16 v[120:121], v203 offset:4160
	ds_read_b64_tr_b16 v[124:125], v203 offset:4224
	ds_read_b64_tr_b16 v[122:123], v203 offset:64
	ds_read_b128 v[126:129], v204
	ds_read_b64_tr_b16 v[210:211], v205
	ds_read_b64_tr_b16 v[212:213], v205 offset:4160
	ds_read_b64_tr_b16 v[216:217], v205 offset:4224
	ds_read_b64_tr_b16 v[214:215], v205 offset:64
	s_waitcnt lgkmcnt(7)
	v_mfma_f32_32x32x16_bf16 v[18:33], v[114:117], v[118:121], v[18:33]
	s_waitcnt lgkmcnt(5)
	v_mfma_f32_32x32x16_bf16 v[2:17], v[114:117], v[122:125], v[2:17]
	s_waitcnt lgkmcnt(2)
	v_mfma_f32_32x32x16_bf16 v[18:33], v[126:129], v[210:213], v[18:33]
	s_waitcnt lgkmcnt(0)
	v_mfma_f32_32x32x16_bf16 v[2:17], v[126:129], v[214:217], v[2:17]
	s_waitcnt lgkmcnt(0)
	s_barrier
	v_add_u32_e32 v126, 0x11480, v209
	ds_read_b128 v[114:117], v126
	ds_read_b128 v[118:121], v126 offset:32
	ds_read_b128 v[122:125], v126 offset:64
	ds_read_b128 v[126:129], v126 offset:96
	s_ashr_i32 s39, s38, 31
	s_waitcnt lgkmcnt(3)
	s_nop 1
	v_mul_f32_e32 v18, v18, v114
	s_nop 0
	v_mul_f32_e32 v2, v2, v114
	v_cvt_pk_bf16_f32 v18, v18, s0
	v_cvt_pk_bf16_f32 v2, v2, s0
	ds_write_b16 v187, v18
	v_mul_f32_e32 v18, v19, v115
	ds_write_b16 v188, v2
	v_mul_f32_e32 v2, v3, v115
	v_cvt_pk_bf16_f32 v18, v18, s0
	v_cvt_pk_bf16_f32 v2, v2, s0
	ds_write_b16 v187, v18 offset:1040
	v_mul_f32_e32 v18, v20, v116
	ds_write_b16 v188, v2 offset:1040
	v_mul_f32_e32 v2, v4, v116
	v_cvt_pk_bf16_f32 v18, v18, s0
	v_cvt_pk_bf16_f32 v2, v2, s0
	ds_write_b16 v187, v18 offset:2080
	v_mul_f32_e32 v18, v21, v117
	ds_write_b16 v188, v2 offset:2080
	v_mul_f32_e32 v2, v5, v117
	v_cvt_pk_bf16_f32 v18, v18, s0
	v_cvt_pk_bf16_f32 v2, v2, s0
	ds_write_b16 v187, v18 offset:3120
	s_waitcnt lgkmcnt(9)
	v_mul_f32_e32 v18, v22, v118
	ds_write_b16 v188, v2 offset:3120
	v_mul_f32_e32 v2, v6, v118
	v_cvt_pk_bf16_f32 v18, v18, s0
	v_cvt_pk_bf16_f32 v2, v2, s0
	ds_write_b16 v187, v18 offset:8320
	v_mul_f32_e32 v18, v23, v119
	ds_write_b16 v188, v2 offset:8320
	v_mul_f32_e32 v2, v7, v119
	v_cvt_pk_bf16_f32 v18, v18, s0
	v_cvt_pk_bf16_f32 v2, v2, s0
	ds_write_b16 v187, v18 offset:9360
	v_mul_f32_e32 v18, v24, v120
	ds_write_b16 v188, v2 offset:9360
	v_mul_f32_e32 v2, v8, v120
	v_cvt_pk_bf16_f32 v18, v18, s0
	v_cvt_pk_bf16_f32 v2, v2, s0
	ds_write_b16 v187, v18 offset:10400
	v_mul_f32_e32 v18, v25, v121
	ds_write_b16 v188, v2 offset:10400
	v_mul_f32_e32 v2, v9, v121
	v_cvt_pk_bf16_f32 v18, v18, s0
	v_cvt_pk_bf16_f32 v2, v2, s0
	ds_write_b16 v187, v18 offset:11440
	s_waitcnt lgkmcnt(14)
	v_mul_f32_e32 v18, v26, v122
	ds_write_b16 v188, v2 offset:11440
	v_mul_f32_e32 v2, v10, v122
	v_cvt_pk_bf16_f32 v18, v18, s0
	v_cvt_pk_bf16_f32 v2, v2, s0
	ds_write_b16 v187, v18 offset:16640
	v_mul_f32_e32 v18, v27, v123
	ds_write_b16 v188, v2 offset:16640
	v_mul_f32_e32 v2, v11, v123
	v_cvt_pk_bf16_f32 v18, v18, s0
	v_cvt_pk_bf16_f32 v2, v2, s0
	ds_write_b16 v187, v18 offset:17680
	v_mul_f32_e32 v18, v28, v124
	ds_write_b16 v188, v2 offset:17680
	v_mul_f32_e32 v2, v12, v124
	v_cvt_pk_bf16_f32 v18, v18, s0
	v_cvt_pk_bf16_f32 v2, v2, s0
	ds_write_b16 v187, v18 offset:18720
	v_mul_f32_e32 v18, v29, v125
	ds_write_b16 v188, v2 offset:18720
	v_mul_f32_e32 v2, v13, v125
	v_cvt_pk_bf16_f32 v18, v18, s0
	v_cvt_pk_bf16_f32 v2, v2, s0
	ds_write_b16 v187, v18 offset:19760
	v_mul_f32_e32 v18, v30, v126
	ds_write_b16 v188, v2 offset:19760
	v_mul_f32_e32 v2, v14, v126
	v_cvt_pk_bf16_f32 v18, v18, s0
	v_cvt_pk_bf16_f32 v2, v2, s0
	ds_write_b16 v187, v18 offset:24960
	v_mul_f32_e32 v18, v31, v127
	ds_write_b16 v188, v2 offset:24960
	v_mul_f32_e32 v2, v15, v127
	v_cvt_pk_bf16_f32 v18, v18, s0
	v_cvt_pk_bf16_f32 v2, v2, s0
	ds_write_b16 v187, v18 offset:26000
	v_mul_f32_e32 v18, v32, v128
	ds_write_b16 v188, v2 offset:26000
	v_mul_f32_e32 v2, v16, v128
	v_cvt_pk_bf16_f32 v18, v18, s0
	v_cvt_pk_bf16_f32 v2, v2, s0
	ds_write_b16 v187, v18 offset:27040
	v_mul_f32_e32 v18, v33, v129
	ds_write_b16 v188, v2 offset:27040
	v_mul_f32_e32 v2, v17, v129
	v_cvt_pk_bf16_f32 v18, v18, s0
	v_cvt_pk_bf16_f32 v2, v2, s0
	ds_write_b16 v187, v18 offset:28080
	ds_write_b16 v188, v2 offset:28080
	s_waitcnt lgkmcnt(0)
	s_barrier
	ds_read_b128 v[2:5], v189
	ds_read_b128 v[6:9], v190
	s_lshl_b64 s[6:7], s[38:39], 15
	v_lshl_add_u64 v[14:15], v[138:139], 0, s[6:7]
	v_lshl_add_u64 v[10:11], v[140:141], 1, v[14:15]
	s_waitcnt lgkmcnt(1)
	global_store_dwordx4 v[10:11], v[2:5], off
	ds_read_b128 v[2:5], v191
	ds_read_b128 v[10:13], v192
	v_lshl_add_u64 v[16:17], v[142:143], 1, v[14:15]
	s_waitcnt lgkmcnt(2)
	global_store_dwordx4 v[16:17], v[6:9], off
	s_addk_i32 s56, 0xff40
	s_cmpk_lg_i32 s56, 0xbf
	v_lshl_add_u64 v[6:7], v[144:145], 1, v[14:15]
	s_waitcnt lgkmcnt(1)
	global_store_dwordx4 v[6:7], v[2:5], off
	s_mov_b32 s38, s48
	v_mov_b32_e32 v208, v207
	v_lshl_add_u64 v[2:3], v[146:147], 1, v[14:15]
	s_waitcnt lgkmcnt(0)
	global_store_dwordx4 v[2:3], v[10:13], off
	s_mov_b32 s98, 1
	s_cbranch_scc0 .LBB0_2085

.LBB0_2051:
	s_lshl_b32 s36, s52, 10
	s_cmp_lg_u32 s98, 0
	s_cbranch_scc1 .Lat_c0_steady
	s_waitcnt vmcnt(15)
	ds_write_b128 v193, v[50:53]
	s_waitcnt vmcnt(14)
	ds_write_b128 v193, v[54:57] offset:1040
	s_waitcnt vmcnt(13)
	ds_write_b128 v193, v[58:61] offset:2080
	s_waitcnt vmcnt(12)
	ds_write_b128 v193, v[62:65] offset:3120
	s_waitcnt vmcnt(11)
	ds_write_b128 v193, v[66:69] offset:4160
	s_waitcnt vmcnt(10)
	ds_write_b128 v193, v[70:73] offset:5200
	s_waitcnt vmcnt(9)
	ds_write_b128 v193, v[82:85] offset:6240
	s_waitcnt vmcnt(8)
	ds_write_b128 v193, v[86:89] offset:7280
	s_branch .Lat_c0_done
.Lat_c0_steady:
	s_waitcnt vmcnt(23)
	ds_write_b128 v193, v[50:53]
	s_waitcnt vmcnt(22)
	ds_write_b128 v193, v[54:57] offset:1040
	s_waitcnt vmcnt(21)
	ds_write_b128 v193, v[58:61] offset:2080
	s_waitcnt vmcnt(20)
	ds_write_b128 v193, v[62:65] offset:3120
	s_waitcnt vmcnt(19)
	ds_write_b128 v193, v[66:69] offset:4160
	s_waitcnt vmcnt(18)
	ds_write_b128 v193, v[70:73] offset:5200
	s_waitcnt vmcnt(17)
	ds_write_b128 v193, v[82:85] offset:6240
	s_waitcnt vmcnt(16)
	ds_write_b128 v193, v[86:89] offset:7280
.Lat_c0_done:
	s_add_i32 s11, s54, s36
	s_waitcnt lgkmcnt(0)
	s_barrier
	v_mov_b32_e32 v6, s11
	ds_read_b128 v[2:5], v6 offset:512
	ds_read_b128 v[6:9], v6 offset:528
	s_waitcnt lgkmcnt(1)
	v_readfirstlane_b32 s6, v2
	s_lshl_b32 s6, s6, 10
	v_readfirstlane_b32 s7, v3
	s_lshl_b32 s7, s7, 10
	s_nop 1
	buffer_load_dwordx4 v[50:53], v132, s[12:15], s6 offen
	s_nop 0
	buffer_load_dwordx4 v[54:57], v132, s[12:15], s7 offen
	v_readfirstlane_b32 s6, v4
	s_lshl_b32 s6, s6, 10
	v_readfirstlane_b32 s7, v5
	s_lshl_b32 s7, s7, 10
	s_nop 1
	buffer_load_dwordx4 v[58:61], v132, s[12:15], s6 offen
	s_nop 0
	buffer_load_dwordx4 v[62:65], v132, s[12:15], s7 offen
	s_waitcnt lgkmcnt(0)
	v_readfirstlane_b32 s6, v6
	s_lshl_b32 s6, s6, 10
	v_readfirstlane_b32 s7, v7
	s_lshl_b32 s7, s7, 10
	s_nop 1
	buffer_load_dwordx4 v[66:69], v132, s[12:15], s6 offen
	s_nop 0
	buffer_load_dwordx4 v[70:73], v132, s[12:15], s7 offen
	v_readfirstlane_b32 s6, v8
	s_lshl_b32 s6, s6, 10
	v_readfirstlane_b32 s7, v9
	s_lshl_b32 s7, s7, 10
	s_nop 1
	buffer_load_dwordx4 v[82:85], v132, s[12:15], s6 offen
	s_nop 0
	buffer_load_dwordx4 v[86:89], v132, s[12:15], s7 offen
	ds_read_b128 v[2:5], v194
	ds_read_b128 v[6:9], v194 offset:64
	ds_read_b128 v[10:13], v194 offset:16640
	ds_read_b128 v[14:17], v194 offset:16704
	ds_read_b128 v[18:21], v194 offset:33280
	ds_read_b128 v[22:25], v194 offset:33344
	ds_read_b128 v[26:29], v194 offset:49920
	ds_read_b128 v[30:33], v194 offset:49984
	s_waitcnt vmcnt(15) lgkmcnt(7)
	v_mfma_f32_16x16x32_bf16 v[2:5], v[2:5], v[34:37], 0
	s_waitcnt lgkmcnt(5)
	v_mfma_f32_16x16x32_bf16 v[10:13], v[10:13], v[34:37], 0
	s_waitcnt lgkmcnt(3)
	v_mfma_f32_16x16x32_bf16 v[18:21], v[18:21], v[34:37], 0
	s_waitcnt lgkmcnt(1)
	v_mfma_f32_16x16x32_bf16 v[26:29], v[26:29], v[34:37], 0
	s_waitcnt vmcnt(14)
	v_mfma_f32_16x16x32_bf16 v[2:5], v[6:9], v[38:41], v[2:5]
	v_mfma_f32_16x16x32_bf16 v[6:9], v[14:17], v[38:41], v[10:13]
	v_mfma_f32_16x16x32_bf16 v[10:13], v[22:25], v[38:41], v[18:21]
	s_waitcnt lgkmcnt(0)
	v_mfma_f32_16x16x32_bf16 v[14:17], v[30:33], v[38:41], v[26:29]
	s_nop 0
	ds_read_b128 v[18:21], v194 offset:128
	ds_read_b128 v[22:25], v194 offset:192
	ds_read_b128 v[26:29], v194 offset:16768
	ds_read_b128 v[30:33], v194 offset:16832
	ds_read_b128 v[114:117], v194 offset:33408
	ds_read_b128 v[118:121], v194 offset:33472
	ds_read_b128 v[122:125], v194 offset:50048
	ds_read_b128 v[126:129], v194 offset:50112
	s_waitcnt vmcnt(13) lgkmcnt(7)
	v_mfma_f32_16x16x32_bf16 v[2:5], v[18:21], v[42:45], v[2:5]
	s_waitcnt lgkmcnt(5)
	v_mfma_f32_16x16x32_bf16 v[6:9], v[26:29], v[42:45], v[6:9]
	s_waitcnt lgkmcnt(3)
	v_mfma_f32_16x16x32_bf16 v[18:21], v[114:117], v[42:45], v[10:13]
	s_waitcnt lgkmcnt(1)
	v_mfma_f32_16x16x32_bf16 v[26:29], v[122:125], v[42:45], v[14:17]
	s_waitcnt vmcnt(12)
	v_mfma_f32_16x16x32_bf16 v[14:17], v[22:25], v[46:49], v[2:5]
	v_mfma_f32_16x16x32_bf16 v[10:13], v[30:33], v[46:49], v[6:9]
	v_mfma_f32_16x16x32_bf16 v[6:9], v[118:121], v[46:49], v[18:21]
	s_waitcnt lgkmcnt(0)
	v_mfma_f32_16x16x32_bf16 v[2:5], v[126:129], v[46:49], v[26:29]
	s_nop 0
	v_cndmask_b32_e64 v18, 0, 1, s[40:41]
	v_cmp_ne_u32_e64 s[8:9], 1, v18
	s_andn2_b64 vcc, exec, s[40:41]
	v_add_u32_e32 v212, 0x12700, v195
	v_add_u32_e32 v213, 0x12b00, v195
	v_add_u32_e32 v214, 0x12f00, v195
	v_add_u32_e32 v215, 0x13300, v195
	s_cbranch_vccnz .LBB0_2053
	ds_write_b128 v212, v[14:17]
	ds_write_b128 v213, v[10:13]
	ds_write_b128 v214, v[6:9]
	ds_write_b128 v215, v[2:5]

.LBB0_2076:
	s_waitcnt lgkmcnt(0)
	s_barrier
	s_nop 0
	ds_read_b128 v[114:117], v216 offset:96
	ds_read_b128 v[118:121], v216 offset:64
	ds_read_b128 v[122:125], v216 offset:32
	ds_read_b128 v[126:129], v216
	s_waitcnt lgkmcnt(3)
	v_pk_mul_f32 v[30:31], v[30:31], v[114:115]
	v_pk_mul_f32 v[32:33], v[32:33], v[116:117]
	v_pk_mul_f32 v[14:15], v[14:15], v[114:115]
	v_pk_mul_f32 v[16:17], v[16:17], v[116:117]
	ds_read_b128 v[114:117], v211
	ds_read_b64_tr_b16 v[220:221], v199
	ds_read_b64_tr_b16 v[222:223], v199 offset:4160
	ds_read_b64_tr_b16 v[226:227], v199 offset:4224
	ds_read_b64_tr_b16 v[224:225], v199 offset:64
	ds_read_b128 v[228:231], v200
	ds_read_b64_tr_b16 v[232:233], v201
	ds_read_b64_tr_b16 v[234:235], v201 offset:4160
	ds_read_b64_tr_b16 v[238:239], v201 offset:4224
	ds_read_b64_tr_b16 v[236:237], v201 offset:64
	s_waitcnt lgkmcnt(12)
	v_pk_mul_f32 v[26:27], v[26:27], v[118:119]
	s_waitcnt lgkmcnt(11)
	v_pk_mul_f32 v[22:23], v[22:23], v[122:123]
	v_pk_mul_f32 v[28:29], v[28:29], v[120:121]
	v_pk_mul_f32 v[24:25], v[24:25], v[124:125]
	s_waitcnt lgkmcnt(10)
	v_pk_mul_f32 v[20:21], v[20:21], v[128:129]
	v_pk_mul_f32 v[18:19], v[18:19], v[126:127]
	v_pk_mul_f32 v[10:11], v[10:11], v[118:119]
	v_pk_mul_f32 v[6:7], v[6:7], v[122:123]
	v_pk_mul_f32 v[12:13], v[12:13], v[120:121]
	v_pk_mul_f32 v[8:9], v[8:9], v[124:125]
	v_pk_mul_f32 v[4:5], v[4:5], v[128:129]
	v_pk_mul_f32 v[2:3], v[2:3], v[126:127]
	s_waitcnt lgkmcnt(7)
	v_mfma_f32_32x32x16_bf16 v[18:33], v[114:117], v[220:223], v[18:33]
	s_waitcnt lgkmcnt(5)
	v_mfma_f32_32x32x16_bf16 v[2:17], v[114:117], v[224:227], v[2:17]
	s_waitcnt lgkmcnt(2)
	v_mfma_f32_32x32x16_bf16 v[18:33], v[228:231], v[232:235], v[18:33]
	s_waitcnt lgkmcnt(0)
	v_mfma_f32_32x32x16_bf16 v[2:17], v[228:231], v[236:239], v[2:17]
	ds_read_b128 v[114:117], v202
	ds_read_b64_tr_b16 v[118:119], v203
	ds_read_b64_tr_b16 v[120:121], v203 offset:4160
	ds_read_b64_tr_b16 v[124:125], v203 offset:4224
	ds_read_b64_tr_b16 v[122:123], v203 offset:64
	ds_read_b128 v[126:129], v204
	ds_read_b64_tr_b16 v[220:221], v205
	ds_read_b64_tr_b16 v[222:223], v205 offset:4160
	ds_read_b64_tr_b16 v[226:227], v205 offset:4224
	ds_read_b64_tr_b16 v[224:225], v205 offset:64
	s_waitcnt lgkmcnt(7)
	v_mfma_f32_32x32x16_bf16 v[18:33], v[114:117], v[118:121], v[18:33]
	s_waitcnt lgkmcnt(5)
	v_mfma_f32_32x32x16_bf16 v[2:17], v[114:117], v[122:125], v[2:17]
	s_waitcnt lgkmcnt(2)
	v_mfma_f32_32x32x16_bf16 v[18:33], v[126:129], v[220:223], v[18:33]
	s_waitcnt lgkmcnt(0)
	v_mfma_f32_32x32x16_bf16 v[2:17], v[126:129], v[224:227], v[2:17]
	s_waitcnt lgkmcnt(0)
	s_barrier
	s_and_b64 vcc, exec, s[10:11]
	s_cbranch_vccnz .Lat_c3_last
	s_waitcnt vmcnt(15)
	ds_write_b128 v193, v[74:77]
	s_waitcnt vmcnt(14)
	ds_write_b128 v193, v[78:81] offset:1040
	s_waitcnt vmcnt(13)
	ds_write_b128 v193, v[90:93] offset:2080
	s_waitcnt vmcnt(12)
	ds_write_b128 v193, v[94:97] offset:3120
	s_waitcnt vmcnt(11)
	ds_write_b128 v193, v[98:101] offset:4160
	s_waitcnt vmcnt(10)
	ds_write_b128 v193, v[102:105] offset:5200
	s_waitcnt vmcnt(9)
	ds_write_b128 v193, v[106:109] offset:6240
	s_waitcnt vmcnt(8)
	ds_write_b128 v193, v[110:113] offset:7280
	s_branch .Lat_c3_done
.Lat_c3_last:
	s_waitcnt vmcnt(7)
	ds_write_b128 v193, v[74:77]
	s_waitcnt vmcnt(6)
	ds_write_b128 v193, v[78:81] offset:1040
	s_waitcnt vmcnt(5)
	ds_write_b128 v193, v[90:93] offset:2080
	s_waitcnt vmcnt(4)
	ds_write_b128 v193, v[94:97] offset:3120
	s_waitcnt vmcnt(3)
	ds_write_b128 v193, v[98:101] offset:4160
	s_waitcnt vmcnt(2)
	ds_write_b128 v193, v[102:105] offset:5200
	s_waitcnt vmcnt(1)
	ds_write_b128 v193, v[106:109] offset:6240
	s_waitcnt vmcnt(0)
	ds_write_b128 v193, v[110:113] offset:7280
.Lat_c3_done:
	s_waitcnt lgkmcnt(0)
	s_barrier
	s_and_b64 vcc, exec, s[10:11]
	s_cbranch_vccnz .LBB0_2078
	s_add_i32 s36, s36, s53
	v_mov_b32_e32 v74, s36
	ds_read_b128 v[90:93], v74 offset:256
	ds_read_b128 v[104:107], v74 offset:272
	s_waitcnt lgkmcnt(1)
	v_readfirstlane_b32 s36, v90
	v_readfirstlane_b32 s37, v91
	s_lshl_b32 s36, s36, 10
	s_lshl_b32 s37, s37, 10
	s_nop 1
	buffer_load_dwordx4 v[74:77], v132, s[12:15], s36 offen
	buffer_load_dwordx4 v[78:81], v132, s[12:15], s37 offen
	v_readfirstlane_b32 s36, v92
	s_lshl_b32 s36, s36, 10
	v_readfirstlane_b32 s37, v93
	s_lshl_b32 s37, s37, 10
	s_nop 1
	buffer_load_dwordx4 v[90:93], v132, s[12:15], s36 offen
	s_nop 0
	buffer_load_dwordx4 v[94:97], v132, s[12:15], s37 offen
	s_waitcnt lgkmcnt(0)
	v_readfirstlane_b32 s36, v104
	s_lshl_b32 s36, s36, 10
	v_readfirstlane_b32 s37, v105
	s_lshl_b32 s37, s37, 10
	s_nop 1
	buffer_load_dwordx4 v[98:101], v132, s[12:15], s36 offen
	s_nop 0
	buffer_load_dwordx4 v[102:105], v132, s[12:15], s37 offen
	v_readfirstlane_b32 s36, v106
	s_lshl_b32 s36, s36, 10
	v_readfirstlane_b32 s37, v107
	s_lshl_b32 s37, s37, 10
	s_nop 1
	buffer_load_dwordx4 v[106:109], v132, s[12:15], s36 offen
	s_nop 0
	buffer_load_dwordx4 v[110:113], v132, s[12:15], s37 offen

.LBB0_2128:
	s_waitcnt vmcnt(0)
	v_max_f32_e32 v10, v177, v177
	v_max_f32_e32 v181, v160, v160
	v_max_f32_e32 v179, v181, v10
	v_sub_f32_e32 v10, v176, v179
	v_mul_f32_e32 v10, 0x3fb8aa3b, v10
	v_exp_f32_e32 v10, v10
	s_bitcmp1_b32 s70, 0
	s_cselect_b32 s0, 0x2400, 0
	s_add_i32 s6, s0, 0
	v_add_u32_e32 v11, s6, v154
	v_lshlrev_b32_e32 v12, 16, v74
	v_and_b32_e32 v13, 0xffff0000, v74
	v_lshlrev_b32_e32 v14, 16, v75
	v_and_b32_e32 v15, 0xffff0000, v75
	v_lshlrev_b32_e32 v16, 16, v76
	v_and_b32_e32 v17, 0xffff0000, v76
	v_lshlrev_b32_e32 v18, 16, v77
	v_and_b32_e32 v19, 0xffff0000, v77
	v_pk_mul_f32 v[14:15], v[10:11], v[14:15] op_sel_hi:[0,1]
	v_pk_mul_f32 v[12:13], v[10:11], v[12:13] op_sel_hi:[0,1]
	v_pk_mul_f32 v[18:19], v[10:11], v[18:19] op_sel_hi:[0,1]
	v_pk_mul_f32 v[16:17], v[10:11], v[16:17] op_sel_hi:[0,1]
	v_cvt_pk_bf16_f32 v12, v12, v13
	v_cvt_pk_bf16_f32 v13, v14, v15
	v_cvt_pk_bf16_f32 v14, v16, v17
	v_cvt_pk_bf16_f32 v15, v18, v19
	v_add_u32_e32 v178, 0, v154
	ds_write_b128 v172, v[58:61]
	ds_write_b128 v173, v[62:65]
	ds_write_b128 v174, v[66:69]
	ds_write_b128 v175, v[70:73]
	ds_write_b128 v11, v[74:77] offset:33792
	ds_write_b128 v178, v[12:15] offset:52224
	s_and_saveexec_b64 s[0:1], s[4:5]
	v_cvt_pk_bf16_f32 v10, v10, s0
	v_add_u32_e32 v11, 0, v166
	ds_write_b16 v11, v10 offset:63488
	s_or_b64 exec, exec, s[0:1]
	s_waitcnt lgkmcnt(0)
	s_barrier
	s_add_i32 s0, s35, 0xfffd0000
	s_add_i32 s1, s35, 0xfffe0000
	v_lshl_add_u64 v[10:11], s[76:77], 0, v[150:151]
	buffer_load_dwordx4 v[58:61], v162, s[44:47], s0 offen
	buffer_load_dwordx4 v[62:65], v162, s[44:47], s1 offen
	s_add_i32 s1, s35, 0xffff0000
	s_mov_b32 s50, s46
	s_mov_b32 s51, s47
	v_add_co_u32_e32 v12, vcc, s68, v10
	buffer_load_dwordx4 v[66:69], v162, s[44:47], s1 offen
	buffer_load_dwordx4 v[70:73], v162, s[44:47], s35 offen
	s_add_i32 s1, s35, 0xfffd0040
	buffer_load_dwordx4 v[90:93], v165, s[48:51], s0 offen
	buffer_load_dwordx4 v[82:85], v165, s[48:51], s1 offen
	s_add_i32 s0, s35, 0xfffd0080
	v_addc_co_u32_e32 v13, vcc, -1, v11, vcc
	v_lshl_add_u64 v[114:115], s[76:77], 0, v[156:157]
	s_add_i32 s1, s35, 0xfffd00c0
	buffer_load_dwordx4 v[86:89], v165, s[48:51], s0 offen
	buffer_load_dwordx4 v[78:81], v165, s[48:51], s1 offen
	s_sub_i32 s0, s36, 64
	v_add_co_u32_e32 v114, vcc, s69, v114
	buffer_load_dwordx4 v[74:77], v164, s[56:59], s37 offen
	buffer_load_dwordx4 v[22:25], v167, s[52:55], s0 offen
	buffer_load_dwordx4 v[18:21], v167, s[52:55], s36 offen
	v_addc_co_u32_e32 v115, vcc, -1, v115, vcc
	s_add_u32 s0, s76, 0xfffc0000
	global_load_dwordx4 v[14:17], v[10:11], off offset:-252
	s_nop 0
	global_load_dwordx4 v[10:13], v[12:13], off offset:-252
	s_addc_u32 s1, s77, -1
	global_load_dword v176, v[114:115], off offset:-252
	global_load_dword v180, v151, s[0:1]
	global_load_dword v177, v151, s[76:77]
	ds_read_b128 v[114:117], v163
	ds_read_b128 v[118:121], v163 offset:64
	s_waitcnt lgkmcnt(1)
	v_mfma_f32_16x16x32_bf16 v[114:117], v[110:113], v[114:117], 0
	s_andn2_b64 vcc, exec, s[62:63]
	s_waitcnt lgkmcnt(0)
	v_mfma_f32_16x16x32_bf16 v[114:117], v[130:133], v[118:121], v[114:117]
	ds_read_b128 v[118:121], v163 offset:128
	ds_read_b128 v[122:125], v163 offset:192
	s_waitcnt lgkmcnt(1)
	v_mfma_f32_16x16x32_bf16 v[114:117], v[138:141], v[118:121], v[114:117]
	v_cndmask_b32_e64 v118, 0, 1, s[62:63]
	v_cmp_ne_u32_e64 s[10:11], 1, v118
	s_waitcnt lgkmcnt(0)
	v_mfma_f32_16x16x32_bf16 v[126:129], v[134:137], v[122:125], v[114:117]
	s_cbranch_vccnz .LBB0_2132
	s_nop 2
	v_add_u32_e32 v114, s33, v155
	s_nop 2
	ds_write_b128 v114, v[126:129]

.LBB0_2197:
	s_setprio 0
	s_cmp_lt_i32 s93, 9
	s_cbranch_scc1 .LBB0_2249
	s_waitcnt vmcnt(0)
	v_cmp_eq_u32_e32 vcc, 0, v0
	s_waitcnt vmcnt(0) lgkmcnt(0)
	s_barrier
	s_and_saveexec_b64 s[0:1], vcc
	s_cbranch_execz .LBB0_2248
	v_mov_b32_e32 v1, s70
	s_waitcnt vmcnt(0) expcnt(0) lgkmcnt(0)
	ds_read_b32 v3, v1
	ds_read_b32 v1, v1 offset:4
	s_waitcnt lgkmcnt(1)
	v_cmp_ne_u32_e32 vcc, 0, v3
	s_cbranch_vccnz .LBB0_2216
	v_readlane_b32 s4, v254, 0
	v_readlane_b32 s5, v254, 1
	s_load_dwordx2 s[2:3], s[4:5], 0x4
	s_add_u32 s4, s86, 0x1000
	s_addc_u32 s5, s87, 0
	s_add_u32 s6, s86, 0x1100
	s_addc_u32 s7, s87, 0
	s_add_u32 s8, s86, 0x1200
	s_addc_u32 s9, s87, 0
	s_waitcnt lgkmcnt(0)
	s_mul_i32 s2, s2, s84
	s_add_u32 s10, s86, 0x1300
	s_mul_i32 s2, s2, s3
	s_addc_u32 s11, s87, 0
	s_mov_b32 s3, 1
	v_mov_b32_e32 v17, 0
	s_branch .LBB0_2202

	.amdhsa_kernel _Z10hybrid_fwd4Args
		.amdhsa_group_segment_fixed_size 0
		.amdhsa_private_segment_fixed_size 0
		.amdhsa_kernarg_size 464
		.amdhsa_user_sgpr_count 2
		.amdhsa_user_sgpr_dispatch_ptr 0
		.amdhsa_user_sgpr_queue_ptr 0
		.amdhsa_user_sgpr_kernarg_segment_ptr 1
		.amdhsa_user_sgpr_dispatch_id 0
		.amdhsa_user_sgpr_kernarg_preload_length 0
		.amdhsa_user_sgpr_kernarg_preload_offset 0
		.amdhsa_user_sgpr_private_segment_size 0
		.amdhsa_uses_dynamic_stack 0
		.amdhsa_enable_private_segment 0
		.amdhsa_system_sgpr_workgroup_id_x 1
		.amdhsa_system_sgpr_workgroup_id_y 0
		.amdhsa_system_sgpr_workgroup_id_z 0
		.amdhsa_system_sgpr_workgroup_info 0
		.amdhsa_system_vgpr_workitem_id 0
		.amdhsa_next_free_vgpr 256
		.amdhsa_next_free_sgpr 99
		.amdhsa_accum_offset 256
		.amdhsa_reserve_vcc 1
		.amdhsa_float_round_mode_32 0
		.amdhsa_float_round_mode_16_64 0
		.amdhsa_float_denorm_mode_32 3
		.amdhsa_float_denorm_mode_16_64 3
		.amdhsa_dx10_clamp 1
		.amdhsa_ieee_mode 1
		.amdhsa_fp16_overflow 0
		.amdhsa_tg_split 0
		.amdhsa_exception_fp_ieee_invalid_op 0
		.amdhsa_exception_fp_denorm_src 0
		.amdhsa_exception_fp_ieee_div_zero 0
		.amdhsa_exception_fp_ieee_overflow 0
		.amdhsa_exception_fp_ieee_underflow 0
		.amdhsa_exception_fp_ieee_inexact 0
		.amdhsa_exception_int_div_zero 0
	.end_amdhsa_kernel

amdhsa.kernels:
  - .agpr_count:     0
    .args:
      - .offset:         0
        .size:           208
        .value_kind:     by_value
      - .offset:         208
        .size:           4
        .value_kind:     hidden_block_count_x
      - .offset:         212
        .size:           4
        .value_kind:     hidden_block_count_y
      - .offset:         216
        .size:           4
        .value_kind:     hidden_block_count_z
      - .offset:         220
        .size:           2
        .value_kind:     hidden_group_size_x
      - .offset:         222
        .size:           2
        .value_kind:     hidden_group_size_y
      - .offset:         224
        .size:           2
        .value_kind:     hidden_group_size_z
      - .offset:         226
        .size:           2
        .value_kind:     hidden_remainder_x
      - .offset:         228
        .size:           2
        .value_kind:     hidden_remainder_y
      - .offset:         230
        .size:           2
        .value_kind:     hidden_remainder_z
      - .offset:         248
        .size:           8
        .value_kind:     hidden_global_offset_x
      - .offset:         256
        .size:           8
        .value_kind:     hidden_global_offset_y
      - .offset:         264
        .size:           8
        .value_kind:     hidden_global_offset_z
      - .offset:         272
        .size:           2
        .value_kind:     hidden_grid_dims
      - .offset:         328
        .size:           4
        .value_kind:     hidden_dynamic_lds_size
    .group_segment_fixed_size: 0
    .kernarg_segment_align: 8
    .kernarg_segment_size: 464
    .language:       OpenCL C
    .language_version:
      - 2
      - 0
    .max_flat_workgroup_size: 512
    .name:           _Z10hybrid_fwd4Args
    .private_segment_fixed_size: 0
    .sgpr_count:     105
    .sgpr_spill_count: 78
    .symbol:         _Z10hybrid_fwd4Args.kd
    .uniform_work_group_size: 1
    .uses_dynamic_stack: false
    .vgpr_count:     256
    .vgpr_spill_count: 0
    .wavefront_size: 64
